# KV up-projection units: the per-XCD extra (4th) unit goes to different workgroups than the q up-projection's extra unit (rotated deal inside each XCD)
# speedup vs baseline: 1.0140x; 1.0036x over previous
; #define REP(x) for (int rep_ = 0; rep_ < ((DBL_PH) == (x) ? 2 : 1); ++rep_)
; DEV bool xorder(int U, int i, int& L, int vb) {
;     const int G = gridDim.x;
;     if (G & 7) { L = vb + G * i; return L < U; }
;     const int per = G >> 3, chunk = (U + 7) >> 3, j = (vb % per) + per * i;
;     if (j >= chunk) return false;
;     L = (vb / per) * chunk + j; return L < U;
; }
; __global__ void __launch_bounds__(NTHREADS, 2) fwd(const Params p) {
;     ...
;             { EpiKVup E{&lp, layer};
;               Ring rg{0, 0};
;               REP(31) for (int i = 0;; ++i) { int u; if (!xorder(130 * 6, i, u, vb)) break; const int mt = u / 6, nt = u % 6; int un = 0; const bool hn = xorder(130 * 6, i + 1, un, vb);
;                   gemm_unit<256, 128, 4, 2, 3, EpiKVup, false, 1>((const bf16_t*)(ws + WS_ZC) + 384, 640, nullptr, 0, mt * 256, 1 << 30, (const bf16_t*)(ws + WS_WKV) + (size_t)layer * 768 * 256, 256, nt * 128, 4, lds, E, &rg, hn, (un / 6) * 256, (un % 6) * 128); } }
.LBB0_587:
	v_readlane_b32 s100, v253, 22
	s_nop 1
	s_add_i32 s101, s100, 16
	s_and_b32 s101, s101, 31
	s_sub_i32 s101, s101, s100
	s_cmp_eq_u32 s94, 0x100
	s_cselect_b32 s101, s101, 0
	v_readlane_b32 s2, v254, 63
	s_add_u32 s4, s48, 0x2bda0400
	s_mul_i32 s30, s2, 0x30000
	s_addc_u32 s5, s49, 0
	s_lshl_b64 s[6:7], s[30:31], 1
	v_readlane_b32 s3, v255, 0
	s_add_u32 s2, s48, s6
	s_addc_u32 s3, s49, s7
	s_add_u32 s6, s2, 0xa90100
	s_addc_u32 s7, s3, 0
	s_add_u32 s8, s48, 0x2bda0500
	s_addc_u32 s9, s49, 0
	s_add_u32 s48, s48, 0x2bda0580
	s_addc_u32 s49, s49, 0
	s_add_u32 s46, s46, s50
	s_addc_u32 s47, s47, s51
	s_add_u32 s50, s38, 0x32f60100
	s_addc_u32 s51, s39, 0
	s_add_u32 s52, s38, 0x35800100
	s_addc_u32 s53, s39, 0
	s_mov_b64 s[54:55], -1
	s_mov_b32 s12, 0
	s_mov_b32 s19, 0
	s_mov_b32 s13, 0
	s_branch .LBB0_591

; #define REP(x) for (int rep_ = 0; rep_ < ((DBL_PH) == (x) ? 2 : 1); ++rep_)
; DEV bool xorder(int U, int i, int& L, int vb) {
;     const int G = gridDim.x;
;     if (G & 7) { L = vb + G * i; return L < U; }
;     const int per = G >> 3, chunk = (U + 7) >> 3, j = (vb % per) + per * i;
;     if (j >= chunk) return false;
;     L = (vb / per) * chunk + j; return L < U;
; }
; __global__ void __launch_bounds__(NTHREADS, 2) fwd(const Params p) {
;     ...
;               REP(31) for (int i = 0;; ++i) { int u; if (!xorder(130 * 6, i, u, vb)) break; const int mt = u / 6, nt = u % 6; int un = 0; const bool hn = xorder(130 * 6, i + 1, un, vb);
.LBB0_593:
	s_andn2_b64 vcc, exec, s[42:43]
	s_cbranch_vccnz .LBB0_598
	v_readlane_b32 s2, v253, 22
	s_add_i32 s2, s2, s101
	s_add_i32 s2, s2, s12
	s_cmpk_lt_i32 s2, 0x62
	s_cbranch_scc0 .LBB0_596
	v_readlane_b32 s2, v253, 30
	s_add_i32 s2, s2, s101
	s_add_i32 s2, s2, s12
	s_mov_b64 s[20:21], -1
	v_writelane_b32 v255, s2, 2

; #define REP(x) for (int rep_ = 0; rep_ < ((DBL_PH) == (x) ? 2 : 1); ++rep_)
; DEV bool xorder(int U, int i, int& L, int vb) {
;     const int G = gridDim.x;
;     if (G & 7) { L = vb + G * i; return L < U; }
;     const int per = G >> 3, chunk = (U + 7) >> 3, j = (vb % per) + per * i;
;     if (j >= chunk) return false;
;     L = (vb / per) * chunk + j; return L < U;
; }
; __global__ void __launch_bounds__(NTHREADS, 2) fwd(const Params p) {
;     ...
;               REP(31) for (int i = 0;; ++i) { int u; if (!xorder(130 * 6, i, u, vb)) break; const int mt = u / 6, nt = u % 6; int un = 0; const bool hn = xorder(130 * 6, i + 1, un, vb);
.LBB0_603:
	v_readlane_b32 s2, v253, 29
	s_add_i32 s2, s2, s101
	s_add_i32 s2, s2, s12
	s_cmpk_lt_i32 s2, 0x62
	s_mov_b32 s16, 0
	s_cbranch_scc0 .LBB0_605
	v_readlane_b32 s2, v253, 31
	s_add_i32 s2, s2, s101
	s_add_i32 s16, s2, s12
	s_mov_b64 s[20:21], -1
